# static mixer schedule: LRU chains moved off the GLA slots to slots 13-15; their sparse units (qb 11..9) join the dynamic queue
# speedup vs baseline: 1.0372x; 1.0106x over previous
.LBB0_210:
	s_or_b64 exec, exec, s[0:1]
	s_waitcnt lgkmcnt(0)
	s_barrier
	s_load_dword s5, s[94:95], 0x180
	s_mov_b64 s[0:1], src_shared_base
	v_writelane_b32 v252, s0, 6
	s_mov_b32 s51, 0
	s_movk_i32 s93, 0x180
	v_writelane_b32 v252, s1, 7
	s_waitcnt lgkmcnt(0)
	s_ashr_i32 s7, s5, 3
	v_readlane_b32 s4, v252, 0
	s_ashr_i32 s6, s4, 3
	s_cmpk_lt_i32 s6, 0x120
	s_cselect_b64 s[0:1], -1, 0
	v_writelane_b32 v252, s0, 8
	s_movk_i32 s77, 0x70
	s_mov_b32 s85, 0x800000
	v_writelane_b32 v252, s1, 9
	s_lshl_b32 s0, s4, 4
	s_and_b32 s8, s0, 0x70
	s_mul_hi_i32 s0, s6, 0x38e38e39
	s_lshr_b32 s1, s0, 31
	s_ashr_i32 s0, s0, 2
	s_add_i32 s0, s0, s1
	s_add_i32 s2, s0, s8
	s_mul_i32 s0, s0, 18
	s_sub_i32 s10, s6, s0
	s_ashr_i32 s11, s10, 31
	s_lshl_b64 s[0:1], s[10:11], 19
	v_writelane_b32 v252, s0, 10
	s_waitcnt vmcnt(0)
	v_mov_b32_e32 v3, 0
	v_mov_b32_e32 v220, 0x1000
	v_writelane_b32 v252, s1, 11
	s_mov_b32 s0, s10
	v_writelane_b32 v252, s0, 12
	v_mov_b32_e32 v221, 0x2000
	v_mov_b32_e32 v219, 0x3b808081
	v_writelane_b32 v252, s1, 13
	s_add_i32 s0, s10, -12
	s_cmp_lt_u32 s0, 3
	s_cselect_b64 s[0:1], -1, 0
	v_writelane_b32 v252, s0, 14
	s_ashr_i32 s3, s2, 31
	v_mbcnt_hi_u32_b32 v214, -1, v42
	v_writelane_b32 v252, s1, 15
	s_lshl_b64 s[0:1], s[2:3], 19
	v_writelane_b32 v252, s0, 16
	v_mov_b32_e32 v226, 0x180
	v_mov_b32_e32 v232, 0x100000
	v_writelane_b32 v252, s1, 17
	s_mov_b32 s0, s2
	v_writelane_b32 v252, s0, 18
	v_mov_b32_e32 v227, 0x2080
	v_mov_b32_e32 v228, 0xff61b1e6
	v_writelane_b32 v252, s1, 19
	s_lshl_b32 s0, s2, 8
	s_cmpk_eq_i32 s5, 0x100
	v_writelane_b32 v252, s0, 20
	s_cselect_b64 s[0:1], -1, 0
	s_ashr_i32 s10, s4, 4
	v_writelane_b32 v252, s0, 21
	s_ashr_i32 s11, s10, 31
	s_and_b32 s9, s4, 15
	v_writelane_b32 v252, s1, 22
	s_lshl_b64 s[0:1], s[10:11], 2
	s_getpc_b64 s[2:3]
	s_add_u32 s2, s2, __const._Z4mega6Params.SLOT@rel32@lo+4
	s_addc_u32 s3, s3, __const._Z4mega6Params.SLOT@rel32@hi+12
	s_add_u32 s0, s2, s0
	s_addc_u32 s1, s3, s1
	v_writelane_b32 v252, s0, 23
	s_mov_b32 s2, s10
	v_mov_b32_e32 v233, 0xc8
	v_writelane_b32 v252, s1, 24
	s_lshl_b32 s0, s9, 5
	v_writelane_b32 v252, s0, 25
	s_add_i32 s0, s4, 0xffffff70
	v_writelane_b32 v252, s2, 26
	s_add_i32 s1, s10, -9
	s_cmp_lt_u32 s1, 4
	s_cselect_b32 s0, s0, 0x100000
	v_writelane_b32 v252, s3, 27
	v_writelane_b32 v252, s0, 28
	s_lshl_b32 s0, s9, 3
	s_add_i32 s1, s0, -1
	s_lshl_b32 s0, s9, 2
	v_writelane_b32 v252, s9, 29
	s_sub_i32 s0, s1, s0
	v_writelane_b32 v252, s1, 30
	s_cmpk_lt_i32 s6, 0x100
	v_writelane_b32 v252, s0, 31
	s_cselect_b64 s[0:1], -1, 0
	v_writelane_b32 v252, s0, 32
	v_mov_b32_e32 v234, 0xc0
	s_movk_i32 s91, 0xc0
	v_writelane_b32 v252, s1, 33
	s_lshr_b32 s0, s6, 28
	s_add_i32 s0, s6, s0
	s_ashr_i32 s1, s0, 4
	s_and_b32 s0, s0, -16
	s_sub_i32 s2, s6, s0
	v_writelane_b32 v252, s8, 34
	s_add_i32 s8, s1, s8
	s_add_i32 s3, s2, 18
	s_cmp_lt_i32 s2, 0
	s_cselect_b64 s[0:1], -1, 0
	v_writelane_b32 v252, s0, 35
	s_movk_i32 s33, 0x2400
	s_movk_i32 s96, 0xc00
	v_writelane_b32 v252, s1, 36
	s_and_b64 s[0:1], s[0:1], exec
	s_cselect_b32 s50, s3, s2
	v_writelane_b32 v252, s3, 37
	s_lshl_b64 s[0:1], s[50:51], 19
	s_add_i32 s2, s2, 6
	v_writelane_b32 v252, s0, 38
	s_cmp_lt_u32 s2, 3
	s_movk_i32 s97, 0x60
	v_writelane_b32 v252, s1, 39
	s_cselect_b64 s[0:1], -1, 0
	v_writelane_b32 v252, s0, 40
	s_ashr_i32 s9, s8, 31
	s_mov_b32 s83, 0x2aaaaaab
	v_writelane_b32 v252, s1, 41
	s_lshl_b64 s[0:1], s[8:9], 19
	v_writelane_b32 v252, s0, 42
	s_movk_i32 s86, 0xff40
	s_movk_i32 s87, 0x7fff
	v_writelane_b32 v252, s1, 43
	s_mov_b32 s0, s8
	v_writelane_b32 v252, s0, 44
	s_movk_i32 s88, 0x9ff
	s_movk_i32 s89, 0x2080
	v_writelane_b32 v252, s1, 45
	s_lshl_b32 s0, s8, 8
	s_cmpk_lt_i32 s6, 0x80
	v_writelane_b32 v252, s0, 46
	s_cselect_b64 s[0:1], -1, 0
	v_writelane_b32 v252, s0, 47
	s_mov_b32 s90, 0xff61b1e6
	s_mov_b64 s[60:61], 0x80
	v_writelane_b32 v252, s1, 48
	s_and_b32 s0, s4, 7
	s_cmp_lt_i32 s6, 64
	s_cselect_b64 s[2:3], -1, 0
	v_writelane_b32 v252, s2, 49
	s_mov_b64 s[40:41], 0x2200
	s_mov_b64 s[70:71], 0x2000
	v_writelane_b32 v252, s3, 50
	v_writelane_b32 v252, s0, 51
	s_lshl_b32 s2, s0, 4
	s_lshr_b32 s0, s6, 30
	s_add_i32 s0, s6, s0
	s_ashr_i32 s1, s0, 2
	v_writelane_b32 v252, s2, 52
	s_add_i32 s1, s2, s1
	s_and_b32 s0, s0, -4
	v_writelane_b32 v252, s1, 53
	s_sub_i32 s8, s6, s0
	s_lshl_b32 s0, s5, 3
	v_writelane_b32 v252, s0, 54
	s_mov_b64 s[80:81], 0x48000
	s_mov_b32 s82, 0x3e38aa3b
	v_writelane_b32 v252, s1, 55
	s_lshl_b32 s0, s5, 5
	v_writelane_b32 v252, s0, 56
	s_ashr_i32 s0, s4, 6
	v_writelane_b32 v252, s0, 57
	s_and_b32 s0, s6, 7
	s_cmp_lt_u32 s0, 4
	v_writelane_b32 v252, s0, 58
	s_cselect_b64 s[0:1], -1, 0
	s_abs_i32 s2, s7
	v_cvt_f32_u32_e32 v1, s2
	v_writelane_b32 v252, s0, 59
	s_mov_b32 s5, s51
	s_ashr_i32 s9, s8, 31
	v_rcp_iflag_f32_e32 v1, v1
	v_writelane_b32 v252, s1, 60
	v_writelane_b32 v252, s7, 61
	s_and_b32 s1, s6, 1
	v_mul_f32_e32 v1, 0x4f7ffffe, v1
	v_cvt_u32_f32_e32 v1, v1
	v_writelane_b32 v252, s6, 62
	s_lshl_b32 s4, s1, 7
	v_writelane_b32 v252, s4, 63
	s_lshl_b32 s1, s1, 1
	s_lshl_b32 s0, s6, 18
	v_writelane_b32 v253, s5, 0
	v_writelane_b32 v253, s1, 1
	v_writelane_b32 v253, s2, 2
	s_sub_i32 s1, 0, s2
	v_readfirstlane_b32 s2, v1
	s_mul_i32 s1, s1, s2
	s_mul_hi_u32 s1, s2, s1
	s_add_i32 s1, s2, s1
	v_writelane_b32 v253, s1, 3
	s_add_i32 s1, 0, 0x26280
	v_writelane_b32 v253, s1, 4
	s_add_i32 s1, 0, 0x26284
	v_writelane_b32 v253, s1, 5
	s_add_i32 s1, 0, 0x26288
	v_writelane_b32 v253, s1, 6
	s_add_i32 s1, 0, 0x18400
	v_writelane_b32 v253, s1, 7
	s_add_i32 s1, 0, 0x184c0
	v_writelane_b32 v253, s1, 8
	s_add_i32 s1, 0, 0x17700
	v_writelane_b32 v253, s1, 9
	s_add_i32 s1, 0, 0x17800
	v_writelane_b32 v253, s1, 10
	s_add_i32 s1, 0, 0x17100
	v_writelane_b32 v253, s1, 11
	s_add_i32 s1, 0, 0xb600
	v_writelane_b32 v253, s1, 12
	s_add_i32 s1, 0, 0x1e650
	v_writelane_b32 v253, s1, 13
	s_add_i32 s1, 0, 0x5c00
	v_writelane_b32 v253, s1, 14
	s_add_i32 s1, 0, 0x15940
	v_writelane_b32 v253, s1, 15
	s_add_i32 s1, 0, 0x15840
	v_writelane_b32 v253, s1, 16
	s_add_i32 s1, 0, 0x15f40
	v_writelane_b32 v253, s1, 17
	s_add_i32 s1, 0, 0x15240
	v_writelane_b32 v253, s1, 18
	s_add_i32 s1, 0, 0x11640
	v_writelane_b32 v253, s1, 19
	s_add_i32 s1, 0, 0x14640
	v_writelane_b32 v253, s1, 20
	s_add_i32 s1, 0, 0x14c40
	v_writelane_b32 v253, s1, 21
	s_add_i32 s1, 0, 0x15c40
	v_writelane_b32 v253, s1, 22
	s_add_i32 s1, 0, 0x15d00
	v_writelane_b32 v253, s1, 23
	s_add_i32 s1, 0, 0x15dc0
	v_writelane_b32 v253, s1, 24
	s_add_i32 s1, 0, 0x15e80
	v_writelane_b32 v253, s1, 25
	s_add_i32 s1, 0, 0x7e40
	v_writelane_b32 v253, s1, 26
	s_add_i32 s1, 0, 0x8280
	v_writelane_b32 v253, s1, 27
	s_add_i32 s1, 0, 0xa094
	v_writelane_b32 v253, s1, 28
	s_add_i32 s1, 0, 0x10380
	v_writelane_b32 v253, s1, 29
	s_add_i32 s1, 0, 0x12380
	v_writelane_b32 v253, s1, 30
	s_add_i32 s1, 0, 0x14380
	v_writelane_b32 v253, s1, 31
	s_add_i32 s1, 0, 0x16380
	v_writelane_b32 v253, s1, 32
	s_add_i32 s1, 0, 0x18380
	v_writelane_b32 v253, s1, 33
	s_add_i32 s1, 0, 0x1a380
	v_writelane_b32 v253, s1, 34
	s_add_i32 s1, 0, 0x1c380
	v_writelane_b32 v253, s1, 35
	s_add_i32 s1, 0, 0x1e380
	v_writelane_b32 v253, s1, 36
	s_add_i32 s1, 0, 0x10100
	v_writelane_b32 v253, s1, 37
	s_add_i32 s1, 0, 0x12100
	v_writelane_b32 v253, s1, 38
	s_add_i32 s1, 0, 0x16100
	v_writelane_b32 v253, s1, 39
	s_add_i32 s1, 0, 0x20060
	v_writelane_b32 v253, s1, 40
	s_add_i32 s1, 0, 0x20004
	v_writelane_b32 v253, s1, 41
	s_add_i32 s1, 0, 0x2000c
	v_writelane_b32 v253, s1, 42
	s_add_i32 s1, 0, 0x20014
	v_writelane_b32 v253, s1, 43
	s_add_i32 s1, 0, 0x2001c
	v_writelane_b32 v253, s1, 44
	s_add_i32 s1, 0, 0x20024
	v_writelane_b32 v253, s1, 45
	s_add_i32 s1, 0, 0x2002c
	v_writelane_b32 v253, s1, 46
	s_add_i32 s1, 0, 0x20034
	v_writelane_b32 v253, s1, 47
	s_add_i32 s1, 0, 0x2003c
	v_writelane_b32 v253, s1, 48
	s_add_i32 s1, 0, 0x20044
	v_writelane_b32 v253, s1, 49
	s_add_i32 s1, 0, 0x2004c
	v_writelane_b32 v253, s1, 50
	s_add_i32 s1, 0, 0x20054
	s_and_b32 s0, s0, 0xc0000
	v_writelane_b32 v253, s1, 51
	s_add_i32 s1, 0, 0x2005c
	v_writelane_b32 v253, s1, 52
	s_lshl_b32 s0, s0, 1
	v_writelane_b32 v253, s0, 53
	s_add_i32 s69, 0, 0x14100
	v_mov_b32_e32 v1, 0x358637bd
	v_writelane_b32 v253, s1, 54
	s_mov_b32 s0, 0
	v_writelane_b32 v253, s0, 55
	s_mov_b32 s0, s8
	v_writelane_b32 v253, s0, 56
	s_mov_b64 s[4:5], 0
	s_mov_b32 s84, 0x3b808081
	v_writelane_b32 v253, s1, 57
	s_lshl_b64 s[0:1], s[8:9], 19
	v_writelane_b32 v253, s0, 58
	s_nop 1
	v_writelane_b32 v253, s1, 59
	s_mov_b64 s[0:1], -1
	v_writelane_b32 v253, s0, 60
	s_nop 1
	v_writelane_b32 v253, s1, 61
	v_writelane_b32 v253, s69, 62
	v_writelane_b32 v253, s92, 63
	s_nop 1
	v_writelane_b32 v254, s93, 0
	v_writelane_b32 v254, s94, 1
	s_nop 1
	v_writelane_b32 v254, s95, 2
	s_branch .LBB0_213

.LBB0_289:
	s_or_b64 exec, exec, s[0:1]
	v_readlane_b32 s0, v253, 60
	v_readlane_b32 s1, v253, 61
	s_xor_b64 s[0:1], s[0:1], -1
	v_writelane_b32 v254, s0, 3
	s_waitcnt lgkmcnt(0)
	s_barrier
	v_writelane_b32 v254, s1, 4
	s_xor_b64 s[0:1], s[4:5], -1
	v_writelane_b32 v254, s0, 5
	s_nop 1
	v_writelane_b32 v254, s1, 6
	v_readlane_b32 s0, v252, 21
	v_readlane_b32 s1, v252, 22
	s_andn2_b64 vcc, exec, s[0:1]
	s_cbranch_vccnz .LBB0_291
	v_readlane_b32 s0, v252, 23
	v_readlane_b32 s1, v252, 24
	s_load_dword s4, s[0:1], 0x0
	s_mov_b64 s[0:1], s[94:95]
	s_load_dwordx2 s[0:1], s[0:1], 0x170
	v_readlane_b32 s2, v253, 55
	s_lshl_b32 s2, s2, 10
	v_readlane_b32 s3, v252, 25
	s_or_b32 s50, s2, s3
	s_lshl_b64 s[2:3], s[50:51], 2
	s_waitcnt lgkmcnt(0)
	s_add_u32 s2, s0, s2
	s_addc_u32 s3, s1, s3
	s_add_u32 s0, s2, 0x800
	v_writelane_b32 v254, s2, 13
	s_addc_u32 s1, s3, 0
	s_mov_b32 s42, 0
	v_writelane_b32 v254, s3, 14
	v_writelane_b32 v254, s0, 9
	s_nop 1
	v_writelane_b32 v254, s1, 10
	s_bfe_u32 s0, s4, 0x40014
	v_readlane_b32 s1, v252, 30
	s_add_i32 s1, s1, s0
	s_cmp_lg_u32 s0, 0
	s_mov_b32 s0, 0x100000
	v_writelane_b32 v254, s0, 11
	s_cselect_b32 s2, s1, 0x100000
	s_bfe_u32 s0, s4, 0x30018
	v_readlane_b32 s1, v252, 31
	s_add_i32 s1, s1, s0
	s_cmp_lg_u32 s0, 0
	s_mov_b32 s0, 12
	v_writelane_b32 v254, s0, 16
	s_mov_b32 s0, 4
	v_writelane_b32 v254, s0, 15
	s_mov_b32 s0, 16
	v_writelane_b32 v254, s0, 8
	v_readlane_b32 s0, v252, 28
	s_cselect_b32 s34, s1, 0x100000
	s_nop 0
	v_writelane_b32 v254, s0, 12
	v_readlane_b32 s0, v253, 6
	s_nop 1
	v_writelane_b32 v254, s0, 7
	v_readlane_b32 s0, v252, 29
	s_nop 1
	v_writelane_b32 v254, s0, 17
	s_branch .LBB0_292

__const._Z4mega6Params.SLOT:
	.long	16783360
	.long	33559552
	.long	50335744
	.long	67120129
	.long	4635648
	.long	5250057
	.long	6326283
	.long	7340045
	.long	8404995
	.long	14407
	.long	9352
	.long	12302
	.long	10255
	.long	1056784
	.long	2100426
	.long	3145900
	.size	__const._Z4mega6Params.SLOT, 64

	.type	__hip_cuid_bff49d4d02027889,@object
